# speedup vs baseline: 1.0022x; 1.0022x over previous
.Lmy_noprio:
	s_lshl_b64 s[76:77], s[38:39], 18
	s_waitcnt lgkmcnt(0)
	s_add_u32 s0, s70, s76
	v_bfe_u32 v4, v0, 5, 1
	v_and_b32_e32 v1, 63, v0
	v_writelane_b32 v252, s0, 0
	s_addc_u32 s0, s71, s77
	v_lshlrev_b32_e32 v159, 2, v4
	v_writelane_b32 v252, s0, 1
	v_cmp_gt_u32_e64 s[4:5], 32, v1
	v_sub_u32_e32 v3, v0, v159
	v_mov_b32_e32 v2, 0x3c00
	v_writelane_b32 v252, s4, 2
	v_lshlrev_b32_e32 v3, 2, v3
	v_or_b32_e32 v11, 1, v159
	s_lshl_b32 s40, s33, 16
	v_writelane_b32 v252, s5, 3
	v_cndmask_b32_e64 v2, 0, v2, s[4:5]
	s_lshr_b32 s41, s1, 6
	s_bfe_u32 s5, s2, 0x30003
	v_and_b32_e32 v9, 0x7c, v3
	v_sub_u32_e32 v3, v0, v11
	s_add_u32 s0, s72, s76
	v_lshlrev_b32_e32 v3, 2, v3
	v_or_b32_e32 v166, 2, v159
	v_writelane_b32 v252, s0, 4
	s_addc_u32 s0, s73, s77
	v_and_b32_e32 v12, 0x7c, v3
	v_sub_u32_e32 v3, v0, v166
	v_writelane_b32 v252, s0, 5
	s_lshl_b32 s0, s41, 12
	v_lshlrev_b32_e32 v3, 2, v3
	v_or_b32_e32 v167, 3, v159
	s_lshl_b64 s[2:3], s[38:39], 11
	v_bfe_u32 v5, v0, 4, 2
	s_bfe_u32 s39, s1, 0x20006
	s_add_i32 s0, s0, 0x20000
	v_and_b32_e32 v14, 0x7c, v3
	v_sub_u32_e32 v3, v0, v167
	v_xor_b32_e32 v28, v5, v0
	v_bitop3_b32 v5, v5, v0, 4 bitop3:0x36
	v_writelane_b32 v252, s5, 6
	s_xor_b32 s5, s5, 15
	s_lshl_b32 s48, s39, 5
	v_lshlrev_b32_e32 v3, 2, v3
	v_or_b32_e32 v168, 8, v159
	v_pack_b32_f16 v118, v2, 0
	v_bfe_u32 v2, v0, 3, 3
	v_lshlrev_b32_e32 v28, 4, v28
	v_lshlrev_b32_e32 v5, 4, v5
	s_cmpk_lt_u32 s1, 0x100
	v_and_b32_e32 v16, 0x7c, v3
	v_sub_u32_e32 v3, v0, v168
	v_lshlrev_b32_e32 v27, 7, v2
	v_and_b32_e32 v28, 0x70, v28
	v_and_b32_e32 v5, 0x70, v5
	v_writelane_b32 v252, s5, 7
	s_cselect_b64 s[44:45], -1, 0
	s_lshl_b32 s5, s39, 1
	v_and_b32_e32 v6, 31, v0
	v_lshlrev_b32_e32 v3, 2, v3
	v_or_b32_e32 v169, 9, v159
	v_lshlrev_b32_e32 v2, 12, v2
	v_or_b32_e32 v172, v28, v27
	v_or_b32_e32 v174, v5, v27
	v_lshlrev_b32_e32 v27, 3, v0
	v_writelane_b32 v252, s5, 8
	s_or_b32 s5, s5, 1
	v_and_b32_e32 v18, 0x7c, v3
	v_sub_u32_e32 v3, v0, v169
	v_lshlrev_b32_e32 v26, 9, v4
	v_or_b32_e32 v173, v28, v2
	v_or_b32_e32 v175, v5, v2
	v_and_b32_e32 v28, 0x70, v27
	s_lshl_b32 s6, s5, 10
	v_writelane_b32 v252, s5, 9
	s_lshl_b32 s5, s5, 15
	v_or_b32_e32 v158, s2, v6
	v_lshlrev_b32_e32 v2, 3, v4
	v_lshlrev_b32_e32 v4, 4, v4
	s_movk_i32 s2, 0x60
	v_lshlrev_b32_e32 v3, 2, v3
	v_or_b32_e32 v170, 10, v159
	v_writelane_b32 v252, s5, 10
	v_bitop3_b32 v180, v4, v28, s2 bitop3:0x36
	s_bfe_u32 s2, s41, 0x10001
	v_and_b32_e32 v20, 0x7c, v3
	v_sub_u32_e32 v3, v0, v170
	s_lshl_b32 s50, s39, 11
	v_writelane_b32 v252, s6, 11
	s_or_b32 s2, s2, -6
	v_lshlrev_b32_e32 v3, 2, v3
	v_or_b32_e32 v171, 11, v159
	v_writelane_b32 v252, s2, 12
	s_and_b32 s2, s50, 0x800
	v_and_b32_e32 v22, 0x7c, v3
	v_sub_u32_e32 v3, v0, v171
	v_lshlrev_b32_e32 v29, 4, v1
	s_or_b32 s2, s40, s2
	v_lshlrev_b32_e32 v3, 2, v3
	s_lshl_b32 s49, s39, 16
	s_or_b32 s1, s40, s50
	s_or_b32 s42, s40, s6
	v_mov_b32_e32 v1, s3
	s_or_b32 s3, s50, 0x1000
	v_or_b32_e32 v190, s2, v29
	s_or_b32 s2, s50, 0x1400
	v_and_b32_e32 v24, 0x7c, v3
	v_mov_b32_e32 v3, 0
	v_writelane_b32 v252, s3, 13
	s_mov_b32 s101, s3
	s_cmp_eq_u32 s33, 1
	s_movk_i32 s4, 0x70
	v_mov_b32_e32 v5, v3
	v_writelane_b32 v252, s2, 14
	v_readfirstlane_b32 s100, v190
	s_cselect_b64 s[2:3], -1, 0
	v_lshl_add_u64 v[160:161], s[68:69], 0, v[4:5]
	v_bitop3_b32 v177, v4, v27, s4 bitop3:0x78
	v_bitop3_b32 v178, v4, v28, 32 bitop3:0x36
	v_bitop3_b32 v179, v4, v28, 64 bitop3:0x36
	v_writelane_b32 v252, s2, 15
	v_mov_b32_e32 v4, 2
	v_lshlrev_b32_sdwa v207, v4, v0 dst_sel:DWORD dst_unused:UNUSED_PAD src0_sel:DWORD src1_sel:BYTE_0
	v_writelane_b32 v252, s3, 16
	s_lshl_b32 s2, s38, 7
	v_mov_b32_e32 v4, 0x7ffff81f
	v_bitop3_b32 v0, s2, v4, v0 bitop3:0xc8
	s_and_b32 s2, s2, 0x780
	s_add_u32 s2, s36, s2
	s_addc_u32 s3, s37, 0
	v_lshl_add_u64 v[162:163], s[2:3], 0, v[2:3]
	s_or_b32 s2, s49, 0x8080
	v_writelane_b32 v252, s2, 17
	s_or_b32 s2, s49, 0x80
	s_lshl_b32 s51, s39, 12
	v_writelane_b32 v252, s2, 18
	s_or_b32 s2, s50, 0x2000
	v_writelane_b32 v252, s2, 19
	s_add_u32 s2, s70, 0x400
	v_writelane_b32 v252, s2, 20
	s_addc_u32 s2, s71, 0
	v_writelane_b32 v252, s2, 21
	s_or_b32 s2, s50, 0x4000
	v_writelane_b32 v252, s2, 22
	s_add_u32 s2, s70, 0x4000
	v_writelane_b32 v252, s2, 23
	s_addc_u32 s2, s71, 0
	v_writelane_b32 v252, s2, 24
	s_or_b32 s2, s49, 0x8100
	v_writelane_b32 v252, s2, 25
	s_add_u32 s2, s72, 0x100
	v_writelane_b32 v252, s2, 26
	s_addc_u32 s2, s73, 0
	v_writelane_b32 v252, s2, 27
	v_writelane_b32 v252, s44, 28
	v_cmp_gt_u32_e64 s[52:53], v6, v159
	v_lshlrev_b32_e32 v7, 2, v6
	v_writelane_b32 v252, s45, 29
	v_writelane_b32 v252, s52, 30
	v_lshlrev_b32_e32 v8, 7, v6
	v_or_b32_e32 v10, v9, v8
	v_writelane_b32 v252, s53, 31
	v_writelane_b32 v252, s51, 32
	v_or_b32_e32 v13, v12, v8
	v_or_b32_e32 v15, v14, v8
	v_or_b32_e32 v17, v16, v8
	v_or_b32_e32 v19, v18, v8
	v_or_b32_e32 v21, v20, v8
	v_or_b32_e32 v23, v22, v8
	v_or_b32_e32 v25, v24, v8
	v_or_b32_e32 v176, s40, v8
	v_or3_b32 v181, s0, v26, v7
	v_cmp_gt_u32_e64 s[4:5], v6, v11
	v_or_b32_e32 v182, 16, v159
	v_or_b32_e32 v183, 17, v159
	v_or_b32_e32 v184, 18, v159
	v_or_b32_e32 v185, 19, v159
	v_or_b32_e32 v186, 24, v159
	v_or_b32_e32 v187, 25, v159
	v_or_b32_e32 v188, 26, v159
	v_or_b32_e32 v189, 27, v159
	v_bitop3_b32 v4, v9, 64, v8 bitop3:0x36
	v_bitop3_b32 v5, v12, 64, v8 bitop3:0x36
	v_bitop3_b32 v7, v14, 64, v8 bitop3:0x36
	v_bitop3_b32 v9, v16, 64, v8 bitop3:0x36
	v_bitop3_b32 v11, v18, 64, v8 bitop3:0x36
	v_bitop3_b32 v12, v20, 64, v8 bitop3:0x36
	v_bitop3_b32 v14, v22, 64, v8 bitop3:0x36
	v_bitop3_b32 v8, v24, 64, v8 bitop3:0x36
	v_add_u32_e32 v210, s1, v29
	v_add_u32_e32 v212, s42, v29
	v_writelane_b32 v252, s48, 33
	v_mov_b32_e32 v119, v3
	v_mov_b32_e32 v120, v3
	v_mov_b32_e32 v121, v3
	v_cmp_gt_u32_e64 s[6:7], v6, v166
	v_cmp_gt_u32_e64 s[8:9], v6, v167
	v_cmp_gt_u32_e64 s[10:11], v6, v168
	v_cmp_gt_u32_e64 s[12:13], v6, v169
	v_cmp_gt_u32_e64 s[14:15], v6, v170
	v_cmp_gt_u32_e64 s[16:17], v6, v171
	v_cmp_gt_u32_e64 s[18:19], v6, v182
	v_cmp_gt_u32_e64 s[20:21], v6, v183
	v_cmp_gt_u32_e64 s[22:23], v6, v184
	v_cmp_gt_u32_e64 s[24:25], v6, v185
	v_cmp_gt_u32_e64 s[26:27], v6, v186
	v_cmp_gt_u32_e64 s[28:29], v6, v187
	v_cmp_gt_u32_e64 s[30:31], v6, v188
	v_cmp_gt_u32_e64 s[34:35], v6, v189
	v_or_b32_e32 v191, 32, v159
	v_or_b32_e32 v192, 33, v159
	v_or_b32_e32 v193, 34, v159
	v_or_b32_e32 v194, 35, v159
	v_or_b32_e32 v195, 40, v159
	v_or_b32_e32 v196, 41, v159
	v_or_b32_e32 v197, 42, v159
	v_or_b32_e32 v198, 43, v159
	v_or_b32_e32 v199, 48, v159
	v_or_b32_e32 v200, 49, v159
	v_or_b32_e32 v201, 50, v159
	v_or_b32_e32 v202, 51, v159
	v_or_b32_e32 v203, 56, v159
	v_or_b32_e32 v204, 57, v159
	v_or_b32_e32 v205, 58, v159
	v_or_b32_e32 v206, 59, v159
	v_or_b32_e32 v208, s40, v29
	v_or_b32_e32 v209, s48, v6
	s_mov_b64 s[38:39], -1
	v_add_u32_e32 v211, 0x4000, v210
	v_add_u32_e32 v213, 0x4000, v212
	v_add_u32_e32 v214, s0, v10
	v_add_u32_e32 v215, s0, v13
	v_add_u32_e32 v216, s0, v15
	v_add_u32_e32 v217, s0, v17
	v_add_u32_e32 v218, s0, v19
	v_add_u32_e32 v219, s0, v21
	v_add_u32_e32 v220, s0, v23
	v_add_u32_e32 v221, s0, v25
	v_add_u32_e32 v222, s0, v4
	v_add_u32_e32 v223, s0, v5
	v_add_u32_e32 v224, s0, v7
	v_add_u32_e32 v225, s0, v9
	v_add_u32_e32 v226, s0, v11
	v_add_u32_e32 v227, s0, v12
	v_add_u32_e32 v228, s0, v14
	v_add_u32_e32 v229, s0, v8
	v_mov_b32_e32 v230, 0xf149f2ca
	v_mov_b32_e32 v231, 0x8000
	v_writelane_b32 v252, s49, 34
	v_writelane_b32 v252, s50, 35
	s_branch .LBB2_2

.LBB2_23:
	s_add_i32 s79, s69, 2
	s_cmp_gt_u32 s79, s92
	s_cselect_b64 s[82:83], -1, 0
	s_cmp_le_u32 s79, s92
	s_cselect_b64 s[86:87], -1, 0
	s_and_b64 vcc, exec, s[82:83]
	s_cbranch_vccnz .LBB2_26
	v_readlane_b32 s2, v252, 36
	s_add_i32 s2, s2, s33
	s_ashr_i32 s2, s2, 5
	v_readlane_b32 s3, v252, 12
	s_add_i32 s2, s2, s3
	s_cmp_lt_i32 s2, -1
	s_cbranch_scc1 .LBB2_26
	s_lshl_b32 s36, s2, 12
	s_add_i32 s2, s36, s101
	s_add_u32 s2, s74, s2
	s_addc_u32 s3, s75, 0
	s_and_b32 s37, s36, 0x7000
	s_add_i32 s37, s37, s100
	s_add_i32 m0, s37, 0x8000
	s_add_i32 s36, s36, s101
	global_load_lds_dwordx4 v172, s[2:3]
	s_add_i32 s36, s36, 0x400
	s_add_u32 s2, s74, s36
	s_addc_u32 s3, s75, 0
	s_add_i32 m0, s37, 0x8400
	s_nop 0
	global_load_lds_dwordx4 v174, s[2:3]

.LBB2_38:
	s_waitcnt vmcnt(0)
	s_andn2_b64 vcc, exec, s[84:85]
	s_waitcnt vmcnt(0) lgkmcnt(0)
	s_barrier
	s_cbranch_vccnz .LBB2_53
	s_andn2_b64 vcc, exec, s[86:87]
	s_cbranch_vccnz .LBB2_41
	s_add_u32 s36, s97, s76
	v_readfirstlane_b32 s3, v210
	s_addc_u32 s37, s68, s77
	s_mov_b32 m0, s3
	v_readfirstlane_b32 s3, v211
	global_load_lds_dwordx4 v172, s[36:37]
	s_add_u32 s36, s93, s76
	s_addc_u32 s37, s91, s77
	s_mov_b32 m0, s3
	v_readfirstlane_b32 s3, v212
	global_load_lds_dwordx4 v173, s[36:37]
	s_add_u32 s36, s90, s76
	s_addc_u32 s37, s99, s77
	s_mov_b32 m0, s3
	v_readfirstlane_b32 s3, v213
	global_load_lds_dwordx4 v174, s[36:37]
	s_add_u32 s36, s0, s76
	s_addc_u32 s37, s1, s77
	s_mov_b32 m0, s3
	s_nop 0
	global_load_lds_dwordx4 v175, s[36:37]
.LBB2_41:
	v_readlane_b32 s3, v252, 40
	s_cmp_gt_i32 s69, s3
	s_cbranch_scc1 .LBB2_44
	v_readlane_b32 s3, v252, 36
	s_add_i32 s3, s3, s33
	s_sub_i32 s3, s3, 64
	s_ashr_i32 s3, s3, 5
	v_readlane_b32 s36, v252, 12
	s_add_i32 s3, s3, s36
	s_cmp_lt_i32 s3, -1
	s_cbranch_scc1 .LBB2_44
	s_lshl_b32 s3, s3, 12
	s_add_i32 s36, s3, s101
	s_add_u32 s36, s74, s36
	s_addc_u32 s37, s75, 0
	s_and_b32 s38, s3, 0x7000
	s_add_i32 s38, s38, s100
	s_add_i32 m0, s38, 0x8000
	s_add_i32 s3, s3, s101
	global_load_lds_dwordx4 v172, s[36:37]
	s_add_i32 s3, s3, 0x400
	s_add_u32 s36, s74, s3
	s_addc_u32 s37, s75, 0
	s_add_i32 m0, s38, 0x8400
	s_nop 0
	global_load_lds_dwordx4 v174, s[36:37]
